# warmyoung
# speedup vs baseline: 1.0122x; 1.0122x over previous
_Z11prep_kernelPKfS0_PKiS2_S0_S0_S0_S0_S0_S0_Pc:
	s_getpc_b64 s[36:37]
	s_add_u32 s36, s36, _Z11attn_kernelILi4EEvPKfS1_S1_S1_S1_S1_PKcPf@rel32@lo+4
	s_addc_u32 s37, s37, _Z11attn_kernelILi4EEvPKfS1_S1_S1_S1_S1_PKcPf@rel32@hi+12
	v_and_b32_e32 v192, 63, v0
	v_lshlrev_b32_e32 v192, 7, v192
	v_min_u32_e32 v192, 0x1180, v192
	s_lshr_b32 s4, s2, 2
	v_lshrrev_b32_e32 v2, 6, v0
	s_and_b32 s4, s4, 0x1ffffffe
	s_load_dwordx4 s[28:31], s[0:1], 0x40
	s_load_dwordx8 s[12:19], s[0:1], 0x0
	s_load_dwordx8 s[20:27], s[0:1], 0x20
	s_load_dwordx2 s[32:33], s[0:1], 0x50
	v_and_b32_e32 v1, 15, v0
	s_and_b32 s3, s2, 7
	v_or_b32_e32 v2, s4, v2
	v_lshl_or_b32 v88, v2, 3, s3
	v_cmp_gt_u32_e64 s[10:11], 14, v1
	v_mul_lo_u32 v7, v88, 14
	v_and_b32_e32 v105, 63, v0
	v_cndmask_b32_e64 v6, 13, v1, s[10:11]
	v_add_u32_e32 v2, v7, v6
	v_mul_u32_u24_e32 v4, 12, v2
	v_lshlrev_b32_e32 v5, 2, v6
	v_cmp_gt_u32_e64 s[8:9], 48, v105
	v_cmp_gt_u32_e64 s[6:7], 14, v105
	v_lshlrev_b32_e32 v118, 1, v0
	v_lshrrev_b32_e32 v104, 4, v0
	v_cndmask_b32_e64 v8, 0, v105, s[8:9]
	v_cndmask_b32_e64 v9, 0, v105, s[6:7]
	v_mad_u32_u24 v8, v88, 48, v8
	v_add_lshl_u32 v9, v7, v9, 2
	v_lshlrev_b32_e32 v8, 2, v8
	s_lshl_b32 s2, s2, 3
	s_and_b32 s2, s2, 0x78
	v_and_b32_e32 v106, 30, v118
	v_or_b32_e32 v107, s2, v104
	v_cmp_gt_u32_e64 s[2:3], 23, v106
	v_or_b32_e32 v10, 1, v106
	v_cmp_gt_u32_e64 s[4:5], 23, v10
	v_lshlrev_b32_e32 v11, 7, v106
	v_lshlrev_b32_e32 v10, 7, v10
	v_cndmask_b32_e64 v11, 0, v11, s[2:3]
	v_cndmask_b32_e64 v10, 0, v10, s[4:5]
	v_or_b32_e32 v11, v11, v107
	v_or_b32_e32 v10, v10, v107
	v_lshlrev_b32_e32 v11, 2, v11
	v_lshlrev_b32_e32 v10, 2, v10
	v_lshlrev_b32_e32 v12, 2, v107
	v_lshlrev_b32_e32 v119, 5, v0
	v_lshlrev_b32_e32 v13, 2, v0
	v_and_b32_e32 v109, 12, v13
	v_and_b32_e32 v91, 0xf80, v119
	v_lshl_or_b32 v91, v109, 2, v91
	v_or_b32_e32 v92, 0x1000, v91
	v_lshlrev_b32_e32 v90, 9, v2
	v_and_b32_e32 v16, 48, v0
	v_or_b32_e32 v90, v90, v16
	v_or_b32_e32 v112, 0x80, v0
	v_or_b32_e32 v111, 0x180, v0
	v_or_b32_e32 v108, 0x280, v0
	v_mov_b32_e32 v87, 0
	v_bfe_u32 v110, v0, 4, 2
	s_movk_i32 s34, 0x60
	v_lshrrev_b32_e32 v136, 1, v0
	v_lshrrev_b32_e32 v18, 3, v0
	v_and_b32_e32 v18, 4, v18
	v_and_b32_e32 v19, 24, v0
	v_and_b32_e32 v20, 2, v136
	v_or3_b32 v18, v18, v19, v20
	v_and_or_b32 v136, v136, s34, v18
	v_mul_u32_u24_e32 v18, 0x110, v109
	v_lshl_add_u32 v136, v136, 1, v18
	v_add_u32_e32 v137, 0x1100, v136
	v_add_u32_e32 v138, 0x2200, v136
	v_lshlrev_b32_e32 v18, 9, v88
	v_and_b32_e32 v19, 0x100, v119
	v_lshlrev_b32_e32 v20, 4, v0
	v_and_b32_e32 v20, 48, v20
	v_or3_b32 v139, v18, v19, v20
	v_and_b32_e32 v19, 8, v118
	v_and_b32_e32 v20, 64, v118
	v_or3_b32 v139, v139, v19, v20
	v_lshlrev_b32_e32 v19, 2, v110
	v_and_b32_e32 v20, 4, v19
	v_or_b32_e32 v139, v139, v20
	v_lshl_or_b32 v140, v1, 5, v18
	v_or_b32_e32 v140, v140, v19
	v_add_u32_e32 v140, 0x80000, v140
	v_lshl_or_b32 v141, v88, 4, v1
	v_lshlrev_b32_e32 v141, 3, v141
	v_add_u32_e32 v141, 0x140000, v141
	v_lshlrev_b32_e32 v20, 8, v88
	v_mul_u32_u24_e32 v21, 43, v105
	v_lshrrev_b32_e32 v21, 9, v21
	v_mul_u32_u24_e32 v21, 12, v21
	v_sub_u32_e32 v22, v105, v21
	v_and_b32_e32 v142, 3, v22
	v_lshrrev_b32_e32 v22, 2, v22
	v_mad_u32_u24 v142, v142, 3, v22
	v_add_u32_e32 v142, v142, v21
	v_lshl_add_u32 v142, v142, 2, v20
	v_add_u32_e32 v142, 0x164000, v142
	v_lshl_add_u32 v143, v105, 2, v20
	v_add_u32_e32 v143, 0x164000, v143
	v_lshlrev_b32_e32 v123, 6, v107
	v_lshl_add_u32 v123, v106, 1, v123
	v_add_u32_e32 v123, 0x160000, v123
	v_lshl_add_u32 v122, v1, 4, v20
	v_or_b32_e32 v122, v122, v19
	v_add_u32_e32 v122, 0x100000, v122
	s_waitcnt lgkmcnt(0)
	global_load_dwordx3 v[82:84], v4, s[12:13]
	global_load_dword v85, v5, s[26:27]
	global_load_dword v114, v8, s[18:19]
	global_load_dword v115, v9, s[16:17]
	global_load_dword v116, v11, s[28:29]
	global_load_dword v113, v10, s[28:29]
	global_load_dword v117, v12, s[30:31]
	global_load_dwordx4 v[66:69], v91, s[20:21]
	global_load_dwordx4 v[70:73], v91, s[20:21] offset:64
	global_load_dwordx4 v[74:77], v92, s[20:21]
	global_load_dwordx4 v[78:81], v92, s[20:21] offset:64
	global_load_dwordx4 v[58:61], v91, s[22:23]
	global_load_dwordx4 v[62:65], v91, s[22:23] offset:64
	global_load_dwordx4 v[50:53], v92, s[22:23]
	global_load_dwordx4 v[54:57], v92, s[22:23] offset:64
	global_load_dwordx4 v[42:45], v91, s[24:25]
	global_load_dwordx4 v[46:49], v91, s[24:25] offset:64
	global_load_dwordx4 v[34:37], v92, s[24:25]
	global_load_dwordx4 v[38:41], v92, s[24:25] offset:64
	global_load_dwordx4 v[26:29], v90, s[14:15] nt
	global_load_dwordx4 v[30:33], v90, s[14:15] offset:64 nt
	global_load_dwordx4 v[18:21], v90, s[14:15] offset:128 nt
	global_load_dwordx4 v[22:25], v90, s[14:15] offset:192 nt
	global_load_dwordx4 v[10:13], v90, s[14:15] offset:256 nt
	global_load_dwordx4 v[14:17], v90, s[14:15] offset:320 nt
	global_load_dwordx4 v[2:5], v90, s[14:15] offset:384 nt
	global_load_dwordx4 v[6:9], v90, s[14:15] offset:448 nt
	global_load_dword v192, v192, s[36:37]
	s_waitcnt vmcnt(27)
	v_mov_b32_e32 v90, v83
	v_mov_b32_e32 v91, v84
	v_lshlrev_b32_e32 v86, 2, v110
	s_waitcnt vmcnt(26)
	v_mul_f32_e32 v84, 0x3fb8aa3b, v85
	s_mov_b32 s14, 0x41700000
	v_exp_f32_e32 v84, v84
	v_cndmask_b32_e64 v94, 0, 1.0, s[10:11]
	v_add_f32_e32 v84, 1.0, v84
	v_cmp_lt_f32_e32 vcc, s14, v85
	v_log_f32_e32 v84, v84
	v_cmp_lt_u32_e64 s[12:13], 15, v105
	v_mul_f32_e32 v84, 0x3f317218, v84
	v_cndmask_b32_e32 v84, v84, v85, vcc
	v_mul_f32_e32 v84, 0xbe715bef, v84
	v_mul_f32_e32 v84, 0x3f3504f3, v84
	v_mul_f32_e32 v84, 0x41800000, v84
	v_cndmask_b32_e64 v99, 0, v84, s[10:11]
	v_mul_f32_e32 v101, -2.0, v99
	v_mul_f32_e32 v100, v82, v82
	v_cmp_gt_u32_e32 vcc, 16, v105
	v_fmac_f32_e32 v100, v90, v90
	v_cmp_eq_u32_e64 s[12:13], 0, v110
	v_fmac_f32_e32 v100, v91, v91
	v_cmp_eq_u32_e64 s[14:15], 1, v110
	v_mul_f32_e32 v83, v101, v82
	v_cmp_eq_u32_e64 s[16:17], 2, v110
	v_mul_f32_e32 v84, v101, v90
	v_mul_f32_e32 v85, v101, v91
	v_mul_f32_e32 v89, v99, v100
	v_mul_f32_e32 v92, v82, v94
	v_mul_f32_e32 v93, v90, v94
	v_mul_f32_e32 v95, v91, v94
	v_mul_f32_e32 v96, v100, v94
	v_cvt_pk_fp8_f32 v88, v83, v83
	v_cvt_pk_fp8_f32 v104, v84, v84
	v_cvt_f32_fp8_e32 v97, v88
	v_cvt_f32_fp8_e32 v98, v104
	v_sub_f32_e32 v97, v83, v97
	v_sub_f32_e32 v98, v84, v98
	v_cvt_pk_fp8_f32 v88, v85, v85
	v_cvt_pk_fp8_f32 v104, v99, v99
	v_cvt_f32_fp8_e32 v101, v88
	v_cvt_f32_fp8_e32 v102, v104
	v_sub_f32_e32 v101, v85, v101
	v_sub_f32_e32 v102, v99, v102
	v_cvt_pk_fp8_f32 v88, v89, v89
	v_cvt_pk_fp8_f32 v104, v92, v92
	v_cvt_f32_fp8_e32 v103, v88
	v_cvt_f32_fp8_e32 v120, v104
	v_sub_f32_e32 v103, v89, v103
	v_sub_f32_e32 v120, v92, v120
	v_cvt_pk_fp8_f32 v88, v93, v93
	v_cvt_pk_fp8_f32 v104, v95, v95
	v_cvt_f32_fp8_e32 v121, v88
	v_cvt_f32_fp8_e32 v86, v104
	v_sub_f32_e32 v121, v93, v121
	v_sub_f32_e32 v86, v95, v86
	v_cvt_pk_fp8_f32 v88, v96, v96
	s_nop 0
	v_cvt_f32_fp8_e32 v87, v88
	s_nop 0
	v_sub_f32_e32 v87, v96, v87
	v_cndmask_b32_e64 v124, v89, v85, s[16:17]
	v_cndmask_b32_e64 v124, v124, v98, s[14:15]
	v_cndmask_b32_e64 v124, v124, v83, s[12:13]
	v_cndmask_b32_e64 v125, v103, v99, s[16:17]
	v_cndmask_b32_e64 v125, v125, v84, s[14:15]
	v_cndmask_b32_e64 v125, v125, v97, s[12:13]
	v_cndmask_b32_e64 v126, 0, v102, s[16:17]
	v_cndmask_b32_e64 v126, v126, v85, s[14:15]
	v_cndmask_b32_e64 v126, v126, v83, s[12:13]
	v_cndmask_b32_e64 v127, 0, v99, s[16:17]
	v_cndmask_b32_e64 v127, v127, v101, s[14:15]
	v_cndmask_b32_e64 v127, v127, v84, s[12:13]
	v_cndmask_b32_e64 v128, v94, v86, s[16:17]
	v_cndmask_b32_e64 v128, v128, v93, s[14:15]
	v_cndmask_b32_e64 v128, v128, v92, s[12:13]
	v_cndmask_b32_e64 v129, v94, v96, s[16:17]
	v_cndmask_b32_e64 v129, v129, v121, s[14:15]
	v_cndmask_b32_e64 v129, v129, v92, s[12:13]
	v_cndmask_b32_e64 v130, 0, v96, s[16:17]
	v_cndmask_b32_e64 v130, v130, v95, s[14:15]
	v_cndmask_b32_e64 v130, v130, v120, s[12:13]
	v_cndmask_b32_e64 v131, 0, v87, s[16:17]
	v_cndmask_b32_e64 v131, v131, v95, s[14:15]
	v_cndmask_b32_e64 v131, v131, v93, s[12:13]
	v_cvt_pk_fp8_f32 v119, v124, v125
	v_cvt_pk_fp8_f32 v103, v128, v129
	v_cvt_pk_fp8_f32 v119, v126, v127 op_sel:[0,0,1]
	v_cvt_pk_fp8_f32 v103, v130, v131 op_sel:[0,0,1]
	s_nop 0
	global_store_dword v139, v119, s[32:33] offset:128
	global_store_dword v140, v103, s[32:33] offset:16
	s_and_saveexec_b64 s[0:1], vcc
	s_cbranch_execz .LBB0_14
	v_cvt_f16_f32_e32 v83, v82
	v_cvt_pk_f16_f32 v90, v90, v91
	s_nop 0
	v_alignbit_b32 v91, 0, v90, 16
	v_pack_b32_f16 v90, v83, v90
	global_store_dwordx2 v141, v[90:91], s[32:33]
.LBB0_14:
	s_or_b64 exec, exec, s[0:1]
	s_and_saveexec_b64 s[0:1], s[8:9]
	s_cbranch_execz .LBB0_16
	s_waitcnt vmcnt(27)
	global_store_dword v142, v114, s[32:33]
.LBB0_16:
	s_or_b64 exec, exec, s[0:1]
	s_waitcnt vmcnt(26)
	v_cmp_ne_u32_e32 vcc, 0, v115
	s_and_b64 s[0:1], s[6:7], vcc
	v_cndmask_b32_e64 v91, 0, 1, s[0:1]
	v_cmp_gt_u32_e64 s[0:1], 2, v105
	s_nop 0
	v_cmp_ne_u32_e32 vcc, 0, v91
	s_and_saveexec_b64 s[6:7], s[0:1]
	s_cbranch_execz .LBB0_18
	s_and_b32 s0, vcc_lo, 0x3fff
	v_mov_b32_e32 v90, s0
	global_store_dword v143, v90, s[32:33] offset:192
.LBB0_18:
	s_or_b64 exec, exec, s[6:7]
	s_waitcnt vmcnt(23)
	v_cmp_eq_u32_e32 vcc, 22, v106
	v_cvt_f16_f32_e32 v89, v117
	v_cvt_f16_f32_e32 v88, v116
	v_cvt_f16_f32_e32 v90, v113
	v_cndmask_b32_e64 v88, 0, v88, s[2:3]
	v_cndmask_b32_e32 v89, 0, v89, vcc
	v_cndmask_b32_e64 v89, v89, v90, s[4:5]
	v_pack_b32_f16 v96, v88, v89
	global_store_dword v123, v96, s[32:33]
	s_waitcnt vmcnt(22)
	v_cvt_pk_f16_f32 v66, v66, v70
	v_cvt_pk_f16_f32 v67, v67, v71
	v_cvt_pk_f16_f32 v68, v68, v72
	v_cvt_pk_f16_f32 v69, v69, v73
	ds_write2_b32 v136, v66, v67 offset0:0 offset1:68
	ds_write2_b32 v136, v68, v69 offset0:136 offset1:204
	s_waitcnt vmcnt(20)
	v_cvt_pk_f16_f32 v74, v74, v78
	v_cvt_pk_f16_f32 v75, v75, v79
	v_cvt_pk_f16_f32 v76, v76, v80
	v_cvt_pk_f16_f32 v77, v77, v81
	ds_write2_b32 v136, v74, v75 offset0:32 offset1:100
	ds_write2_b32 v136, v76, v77 offset0:168 offset1:236
	s_waitcnt vmcnt(18)
	v_cvt_pk_f16_f32 v58, v58, v62
	v_cvt_pk_f16_f32 v59, v59, v63
	v_cvt_pk_f16_f32 v60, v60, v64
	v_cvt_pk_f16_f32 v61, v61, v65
	ds_write2_b32 v137, v58, v59 offset0:0 offset1:68
	ds_write2_b32 v137, v60, v61 offset0:136 offset1:204
	s_waitcnt vmcnt(16)
	v_cvt_pk_f16_f32 v50, v50, v54
	v_cvt_pk_f16_f32 v51, v51, v55
	v_cvt_pk_f16_f32 v52, v52, v56
	v_cvt_pk_f16_f32 v53, v53, v57
	ds_write2_b32 v137, v50, v51 offset0:32 offset1:100
	ds_write2_b32 v137, v52, v53 offset0:168 offset1:236
	s_waitcnt vmcnt(14)
	v_cvt_pk_f16_f32 v42, v42, v46
	v_cvt_pk_f16_f32 v43, v43, v47
	v_cvt_pk_f16_f32 v44, v44, v48
	v_cvt_pk_f16_f32 v45, v45, v49
	ds_write2_b32 v138, v42, v43 offset0:0 offset1:68
	ds_write2_b32 v138, v44, v45 offset0:136 offset1:204
	s_waitcnt vmcnt(12)
	v_cvt_pk_f16_f32 v34, v34, v38
	v_cvt_pk_f16_f32 v35, v35, v39
	v_cvt_pk_f16_f32 v36, v36, v40
	v_cvt_pk_f16_f32 v37, v37, v41
	ds_write2_b32 v138, v34, v35 offset0:32 offset1:100
	ds_write2_b32 v138, v36, v37 offset0:168 offset1:236
	s_movk_i32 s0, 0x110
	v_lshlrev_b32_e32 v48, 4, v110
	v_mad_u32_u24 v48, v1, s0, v48
	s_waitcnt lgkmcnt(0)
	s_barrier
	ds_read_b128 v[144:147], v48
	ds_read_b128 v[152:155], v48 offset:4352
	ds_read_b128 v[160:163], v48 offset:8704
	ds_read_b128 v[148:151], v48 offset:64
	ds_read_b128 v[156:159], v48 offset:4416
	ds_read_b128 v[164:167], v48 offset:8768
	ds_read_b128 v[168:171], v48 offset:128
	ds_read_b128 v[176:179], v48 offset:4480
	ds_read_b128 v[184:187], v48 offset:8832
	ds_read_b128 v[172:175], v48 offset:192
	ds_read_b128 v[180:183], v48 offset:4544
	ds_read_b128 v[188:191], v48 offset:8896
	s_waitcnt vmcnt(10)
	v_cvt_pk_f16_f32 v39, v32, v33
	v_cvt_pk_f16_f32 v38, v30, v31
	v_cvt_pk_f16_f32 v37, v28, v29
	v_cvt_pk_f16_f32 v36, v26, v27
	s_waitcnt lgkmcnt(9)
	s_nop 0
	v_mfma_f32_16x16x32_f16 v[124:127], v[144:147], v[36:39], 0
	v_mfma_f32_16x16x32_f16 v[128:131], v[152:155], v[36:39], 0
	v_mfma_f32_16x16x32_f16 v[132:135], v[36:39], v[160:163], 0
	s_waitcnt vmcnt(8)
	v_cvt_pk_f16_f32 v25, v24, v25
	v_cvt_pk_f16_f32 v24, v22, v23
	v_cvt_pk_f16_f32 v23, v20, v21
	v_cvt_pk_f16_f32 v22, v18, v19
	s_waitcnt lgkmcnt(6)
	s_nop 0
	v_mfma_f32_16x16x32_f16 v[124:127], v[148:151], v[22:25], v[124:127]
	v_mfma_f32_16x16x32_f16 v[128:131], v[156:159], v[22:25], v[128:131]
	v_mfma_f32_16x16x32_f16 v[132:135], v[22:25], v[164:167], v[132:135]
	s_waitcnt vmcnt(6)
	v_cvt_pk_f16_f32 v43, v16, v17
	v_cvt_pk_f16_f32 v42, v14, v15
	v_cvt_pk_f16_f32 v41, v12, v13
	v_cvt_pk_f16_f32 v40, v10, v11
	s_waitcnt lgkmcnt(3)
	s_nop 0
	v_mfma_f32_16x16x32_f16 v[124:127], v[168:171], v[40:43], v[124:127]
	v_mfma_f32_16x16x32_f16 v[128:131], v[176:179], v[40:43], v[128:131]
	v_mfma_f32_16x16x32_f16 v[132:135], v[40:43], v[184:187], v[132:135]
	s_waitcnt vmcnt(4)
	v_cvt_pk_f16_f32 v9, v8, v9
	v_cvt_pk_f16_f32 v8, v6, v7
	v_cvt_pk_f16_f32 v7, v4, v5
	v_cvt_pk_f16_f32 v6, v2, v3
	s_waitcnt lgkmcnt(0)
	s_nop 0
	v_mfma_f32_16x16x32_f16 v[124:127], v[172:175], v[6:9], v[124:127]
	v_mfma_f32_16x16x32_f16 v[128:131], v[180:183], v[6:9], v[128:131]
	v_mfma_f32_16x16x32_f16 v[132:135], v[6:9], v[188:191], v[132:135]
	s_nop 5
	v_mul_f32_e32 v96, 0x403504f3, v124
	v_mul_f32_e32 v97, 0x403504f3, v125
	v_mul_f32_e32 v98, 0x403504f3, v126
	v_mul_f32_e32 v99, 0x403504f3, v127
	v_cvt_pk_fp8_f32 v100, v96, v97
	v_cvt_pk_fp8_f32 v100, v98, v99 op_sel:[0,0,1]
	v_mul_f32_e32 v96, 4.0, v128
	v_mul_f32_e32 v97, 4.0, v129
	v_mul_f32_e32 v98, 4.0, v130
	v_mul_f32_e32 v99, 4.0, v131
	v_cvt_pk_fp8_f32 v101, v96, v97
	v_cvt_pk_fp8_f32 v101, v98, v99 op_sel:[0,0,1]
	global_store_dword v140, v100, s[32:33]
	global_store_dword v139, v101, s[32:33]
	v_mul_f32_e32 v96, 4.0, v132
	v_mul_f32_e32 v97, 4.0, v133
	v_mul_f32_e32 v98, 4.0, v134
	v_mul_f32_e32 v99, 4.0, v135
	v_cvt_pk_fp8_f32 v102, v96, v97
	v_cvt_pk_fp8_f32 v102, v98, v99 op_sel:[0,0,1]
	s_nop 0
	global_store_dword v122, v102, s[32:33]
	s_endpgm
